# baseline (speedup 1.0000x reference)
.Lmk_start:
	s_mov_b32 s28, s8
	s_mov_b64 s[30:31], s[4:5]
	s_mov_b64 s[32:33], s[6:7]
	s_mov_b64 s[6:7], s[2:3]
	s_mov_b64 s[34:35], s[2:3]
	s_mov_b32 s2, s28
	s_and_b32 s3, s2, 7
	s_lshr_b32 s4, s2, 3
	s_and_b32 s5, s4, 3
	s_lshl_b32 s3, s3, 2
	s_or_b32 s8, s3, s5
	s_lshr_b32 s9, s4, 2
	v_lshrrev_b32_e32 v127, 6, v0
	v_and_b32_e32 v124, 63, v0
	v_lshlrev_b32_e32 v125, 3, v124
	v_lshlrev_b32_e32 v124, 4, v124
	v_readfirstlane_b32 s12, v127
	v_mov_b32_e32 v120, 0
	v_mov_b32_e32 v121, 0
	v_mov_b32_e32 v122, 0
	v_mov_b32_e32 v123, 0
	s_lshl_b32 s13, s12, 10
	s_lshl_b32 s14, s9, 3
	s_add_u32 s14, s14, s12
	s_mul_i32 s15, s14, 0x1800
	s_mul_i32 s16, s8, 0x12000
	s_add_u32 s16, s16, 0xc0000
	s_add_u32 s16, s16, s13
	s_add_u32 s20, s13, 0x2000
	s_add_u32 s10, s6, s16
	s_addc_u32 s11, s7, 0
	s_add_u32 s18, s6, s15
	s_addc_u32 s19, s7, 0
	s_add_u32 s22, s18, 0xc00
	s_addc_u32 s23, s19, 0
	s_cmp_lt_u32 s12, 4
	s_cbranch_scc0 .Lmk_vb
	s_mov_b32 m0, s13
	s_nop 0
	global_load_lds_dwordx4 v124, s[10:11]
	s_add_u32 s26, s10, 0x2000
	s_addc_u32 s27, s11, 0
	s_mov_b32 m0, s20
	s_nop 0
	global_load_lds_dwordx4 v124, s[26:27]
	global_load_dwordx4 v[96:99], v124, s[18:19]
	global_load_dwordx4 v[100:103], v124, s[18:19] offset:1024
	global_load_dwordx4 v[104:107], v124, s[18:19] offset:2048
	global_load_dwordx4 v[108:111], v124, s[22:23]
	global_load_dwordx4 v[112:115], v124, s[22:23] offset:1024
	global_load_dwordx4 v[116:119], v124, s[22:23] offset:2048
	s_add_u32 s24, s10, 0x3000
	s_addc_u32 s25, s11, 0
	s_add_u32 s26, s13, 0x3000
	s_mov_b32 m0, s26
	s_nop 0
	global_load_lds_dwordx4 v124, s[24:25]
	s_add_u32 s26, s24, 0x2000
	s_addc_u32 s27, s25, 0
	s_add_u32 s29, s20, 0x3000
	s_mov_b32 m0, s29
	s_nop 0
	global_load_lds_dwordx4 v124, s[26:27]
	s_add_u32 s24, s10, 0x6000
	s_addc_u32 s25, s11, 0
	s_add_u32 s26, s13, 0x6000
	s_mov_b32 m0, s26
	s_nop 0
	global_load_lds_dwordx4 v124, s[24:25]
	s_add_u32 s26, s24, 0x2000
	s_addc_u32 s27, s25, 0
	s_add_u32 s29, s20, 0x6000
	s_mov_b32 m0, s29
	s_nop 0
	global_load_lds_dwordx4 v124, s[26:27]
	s_add_u32 s24, s10, 0x9000
	s_addc_u32 s25, s11, 0
	s_add_u32 s26, s13, 0x9000
	s_mov_b32 m0, s26
	s_nop 0
	global_load_lds_dwordx4 v124, s[24:25]
	s_add_u32 s26, s24, 0x2000
	s_addc_u32 s27, s25, 0
	s_add_u32 s29, s20, 0x9000
	s_mov_b32 m0, s29
	s_nop 0
	global_load_lds_dwordx4 v124, s[26:27]
	s_add_u32 s24, s10, 0xc000
	s_addc_u32 s25, s11, 0
	s_add_u32 s26, s13, 0xc000
	s_mov_b32 m0, s26
	s_nop 0
	global_load_lds_dwordx4 v124, s[24:25]
	s_add_u32 s26, s24, 0x2000
	s_addc_u32 s27, s25, 0
	s_add_u32 s29, s20, 0xc000
	s_mov_b32 m0, s29
	s_nop 0
	global_load_lds_dwordx4 v124, s[26:27]
	s_waitcnt vmcnt(8)
	s_barrier
	ds_read_b128 v[0:3], v124
	ds_read_b128 v[4:7], v124 offset:1024
	ds_read_b128 v[8:11], v124 offset:2048
	ds_read_b128 v[12:15], v124 offset:3072
	ds_read_b128 v[16:19], v124 offset:4096
	ds_read_b128 v[20:23], v124 offset:5120
	s_waitcnt lgkmcnt(0)
	s_setprio 2
	s_nop 0
	v_mfma_f32_32x32x64_f8f6f4 v[48:63], v[0:5], v[96:101], 0 cbsz:2 blgp:2
	ds_read_b128 v[24:27], v124 offset:6144
	v_mfma_f32_32x32x64_f8f6f4 v[48:63], v[6:11], v[102:107], v[48:63] cbsz:2 blgp:2
	ds_read_b128 v[28:31], v124 offset:7168
	ds_read_b128 v[32:35], v124 offset:8192
	v_mfma_f32_32x32x64_f8f6f4 v[48:63], v[12:17], v[108:113], v[48:63] cbsz:2 blgp:2
	ds_read_b128 v[36:39], v124 offset:9216
	v_mfma_f32_32x32x64_f8f6f4 v[48:63], v[18:23], v[114:119], v[48:63] cbsz:2 blgp:2
	ds_read_b128 v[40:43], v124 offset:10240
	ds_read_b128 v[44:47], v124 offset:11264
	s_waitcnt vmcnt(0) lgkmcnt(0)
	s_barrier
	s_add_u32 s24, s10, 0xf000
	s_addc_u32 s25, s11, 0
	s_mov_b32 m0, s13
	s_nop 0
	global_load_lds_dwordx4 v124, s[24:25]
	s_add_u32 s26, s24, 0x2000
	s_addc_u32 s27, s25, 0
	s_mov_b32 m0, s20
	s_nop 0
	global_load_lds_dwordx4 v124, s[26:27]
	v_mfma_f32_32x32x64_f8f6f4 v[64:79], v[24:29], v[96:101], 0 cbsz:2 blgp:2
	ds_read_b128 v[0:3], v124 offset:12288
	ds_read_b128 v[4:7], v124 offset:13312
	ds_read_b128 v[8:11], v124 offset:14336
	ds_read_b128 v[24:27], v124 offset:18432
	v_mfma_f32_32x32x64_f8f6f4 v[64:79], v[30:35], v[102:107], v[64:79] cbsz:2 blgp:2
	ds_read_b128 v[12:15], v124 offset:15360
	ds_read_b128 v[16:19], v124 offset:16384
	ds_read_b128 v[20:23], v124 offset:17408
	ds_read_b128 v[28:31], v124 offset:19456
	ds_read_b128 v[32:35], v124 offset:20480
	v_exp_f32_e32 v48, v48
	v_exp_f32_e32 v49, v49
	v_exp_f32_e32 v50, v50
	v_exp_f32_e32 v51, v51
	v_mfma_f32_32x32x64_f8f6f4 v[64:79], v[36:41], v[108:113], v[64:79] cbsz:2 blgp:2
	ds_read_b128 v[36:39], v124 offset:21504
	v_exp_f32_e32 v52, v52
	v_exp_f32_e32 v53, v53
	v_exp_f32_e32 v54, v54
	v_exp_f32_e32 v55, v55
	v_pk_add_f32 v[120:121], v[120:121], v[48:49]
	v_pk_add_f32 v[122:123], v[122:123], v[50:51]
	v_mfma_f32_32x32x64_f8f6f4 v[64:79], v[42:47], v[114:119], v[64:79] cbsz:2 blgp:2
	ds_read_b128 v[40:43], v124 offset:22528
	ds_read_b128 v[44:47], v124 offset:23552
	v_exp_f32_e32 v56, v56
	v_exp_f32_e32 v57, v57
	v_exp_f32_e32 v58, v58
	v_exp_f32_e32 v59, v59
	v_pk_add_f32 v[120:121], v[120:121], v[52:53]
	v_pk_add_f32 v[122:123], v[122:123], v[54:55]
	s_waitcnt lgkmcnt(5)
	s_nop 0
	v_mfma_f32_32x32x64_f8f6f4 v[80:95], v[0:5], v[96:101], 0 cbsz:2 blgp:2
	ds_read_b128 v[0:3], v124 offset:24576
	v_exp_f32_e32 v60, v60
	v_exp_f32_e32 v61, v61
	v_exp_f32_e32 v62, v62
	v_exp_f32_e32 v63, v63
	v_pk_add_f32 v[120:121], v[120:121], v[56:57]
	v_pk_add_f32 v[122:123], v[122:123], v[58:59]
	v_mfma_f32_32x32x64_f8f6f4 v[80:95], v[6:11], v[102:107], v[80:95] cbsz:2 blgp:2
	ds_read_b128 v[4:7], v124 offset:25600
	ds_read_b128 v[8:11], v124 offset:26624
	v_exp_f32_e32 v64, v64
	v_exp_f32_e32 v65, v65
	v_exp_f32_e32 v66, v66
	v_exp_f32_e32 v67, v67
	v_pk_add_f32 v[120:121], v[120:121], v[60:61]
	v_pk_add_f32 v[122:123], v[122:123], v[62:63]
	v_mfma_f32_32x32x64_f8f6f4 v[80:95], v[12:17], v[108:113], v[80:95] cbsz:2 blgp:2
	ds_read_b128 v[12:15], v124 offset:27648
	v_exp_f32_e32 v68, v68
	v_exp_f32_e32 v69, v69
	v_exp_f32_e32 v70, v70
	v_exp_f32_e32 v71, v71
	v_pk_add_f32 v[120:121], v[120:121], v[64:65]
	v_pk_add_f32 v[122:123], v[122:123], v[66:67]
	v_mfma_f32_32x32x64_f8f6f4 v[80:95], v[18:23], v[114:119], v[80:95] cbsz:2 blgp:2
	ds_read_b128 v[16:19], v124 offset:28672
	ds_read_b128 v[20:23], v124 offset:29696
	v_exp_f32_e32 v72, v72
	v_exp_f32_e32 v73, v73
	v_exp_f32_e32 v74, v74
	v_exp_f32_e32 v75, v75
	v_pk_add_f32 v[120:121], v[120:121], v[68:69]
	v_pk_add_f32 v[122:123], v[122:123], v[70:71]
	s_waitcnt lgkmcnt(6)
	s_nop 0
	v_mfma_f32_32x32x64_f8f6f4 v[48:63], v[24:29], v[96:101], 0 cbsz:2 blgp:2
	ds_read_b128 v[24:27], v124 offset:30720
	v_exp_f32_e32 v76, v76
	v_exp_f32_e32 v77, v77
	v_exp_f32_e32 v78, v78
	v_exp_f32_e32 v79, v79
	v_pk_add_f32 v[120:121], v[120:121], v[72:73]
	v_pk_add_f32 v[122:123], v[122:123], v[74:75]
	v_mfma_f32_32x32x64_f8f6f4 v[48:63], v[30:35], v[102:107], v[48:63] cbsz:2 blgp:2
	ds_read_b128 v[28:31], v124 offset:31744
	ds_read_b128 v[32:35], v124 offset:32768
	v_exp_f32_e32 v80, v80
	v_exp_f32_e32 v81, v81
	v_exp_f32_e32 v82, v82
	v_exp_f32_e32 v83, v83
	v_pk_add_f32 v[120:121], v[120:121], v[76:77]
	v_pk_add_f32 v[122:123], v[122:123], v[78:79]
	v_mfma_f32_32x32x64_f8f6f4 v[48:63], v[36:41], v[108:113], v[48:63] cbsz:2 blgp:2
	ds_read_b128 v[36:39], v124 offset:33792
	v_exp_f32_e32 v84, v84
	v_exp_f32_e32 v85, v85
	v_exp_f32_e32 v86, v86
	v_exp_f32_e32 v87, v87
	v_pk_add_f32 v[120:121], v[120:121], v[80:81]
	v_pk_add_f32 v[122:123], v[122:123], v[82:83]
	v_mfma_f32_32x32x64_f8f6f4 v[48:63], v[42:47], v[114:119], v[48:63] cbsz:2 blgp:2
	ds_read_b128 v[40:43], v124 offset:34816
	ds_read_b128 v[44:47], v124 offset:35840
	v_exp_f32_e32 v88, v88
	v_exp_f32_e32 v89, v89
	v_exp_f32_e32 v90, v90
	v_exp_f32_e32 v91, v91
	v_pk_add_f32 v[120:121], v[120:121], v[84:85]
	v_pk_add_f32 v[122:123], v[122:123], v[86:87]
	s_setprio 1
	s_waitcnt lgkmcnt(6)
	v_mfma_f32_32x32x64_f8f6f4 v[64:79], v[0:5], v[96:101], 0 cbsz:2 blgp:2
	ds_read_b128 v[0:3], v124 offset:36864
	v_exp_f32_e32 v92, v92
	v_exp_f32_e32 v93, v93
	v_exp_f32_e32 v94, v94
	v_exp_f32_e32 v95, v95
	v_pk_add_f32 v[120:121], v[120:121], v[88:89]
	v_pk_add_f32 v[122:123], v[122:123], v[90:91]
	v_mfma_f32_32x32x64_f8f6f4 v[64:79], v[6:11], v[102:107], v[64:79] cbsz:2 blgp:2
	ds_read_b128 v[4:7], v124 offset:37888
	ds_read_b128 v[8:11], v124 offset:38912
	v_exp_f32_e32 v48, v48
	v_exp_f32_e32 v49, v49
	v_exp_f32_e32 v50, v50
	v_exp_f32_e32 v51, v51
	v_pk_add_f32 v[120:121], v[120:121], v[92:93]
	v_pk_add_f32 v[122:123], v[122:123], v[94:95]
	v_mfma_f32_32x32x64_f8f6f4 v[64:79], v[12:17], v[108:113], v[64:79] cbsz:2 blgp:2
	ds_read_b128 v[12:15], v124 offset:39936
	v_exp_f32_e32 v52, v52
	v_exp_f32_e32 v53, v53
	v_exp_f32_e32 v54, v54
	v_exp_f32_e32 v55, v55
	v_pk_add_f32 v[120:121], v[120:121], v[48:49]
	v_pk_add_f32 v[122:123], v[122:123], v[50:51]
	v_mfma_f32_32x32x64_f8f6f4 v[64:79], v[18:23], v[114:119], v[64:79] cbsz:2 blgp:2
	ds_read_b128 v[16:19], v124 offset:40960
	ds_read_b128 v[20:23], v124 offset:41984
	v_exp_f32_e32 v56, v56
	v_exp_f32_e32 v57, v57
	v_exp_f32_e32 v58, v58
	v_exp_f32_e32 v59, v59
	v_pk_add_f32 v[120:121], v[120:121], v[52:53]
	v_pk_add_f32 v[122:123], v[122:123], v[54:55]
	s_waitcnt lgkmcnt(6)
	s_nop 0
	v_mfma_f32_32x32x64_f8f6f4 v[80:95], v[24:29], v[96:101], 0 cbsz:2 blgp:2
	ds_read_b128 v[24:27], v124 offset:43008
	v_exp_f32_e32 v60, v60
	v_exp_f32_e32 v61, v61
	v_exp_f32_e32 v62, v62
	v_exp_f32_e32 v63, v63
	v_pk_add_f32 v[120:121], v[120:121], v[56:57]
	v_pk_add_f32 v[122:123], v[122:123], v[58:59]
	v_mfma_f32_32x32x64_f8f6f4 v[80:95], v[30:35], v[102:107], v[80:95] cbsz:2 blgp:2
	ds_read_b128 v[28:31], v124 offset:44032
	ds_read_b128 v[32:35], v124 offset:45056
	v_exp_f32_e32 v64, v64
	v_exp_f32_e32 v65, v65
	v_exp_f32_e32 v66, v66
	v_exp_f32_e32 v67, v67
	v_pk_add_f32 v[120:121], v[120:121], v[60:61]
	v_pk_add_f32 v[122:123], v[122:123], v[62:63]
	v_mfma_f32_32x32x64_f8f6f4 v[80:95], v[36:41], v[108:113], v[80:95] cbsz:2 blgp:2
	ds_read_b128 v[36:39], v124 offset:46080
	v_exp_f32_e32 v68, v68
	v_exp_f32_e32 v69, v69
	v_exp_f32_e32 v70, v70
	v_exp_f32_e32 v71, v71
	v_pk_add_f32 v[120:121], v[120:121], v[64:65]
	v_pk_add_f32 v[122:123], v[122:123], v[66:67]
	v_mfma_f32_32x32x64_f8f6f4 v[80:95], v[42:47], v[114:119], v[80:95] cbsz:2 blgp:2
	ds_read_b128 v[40:43], v124 offset:47104
	ds_read_b128 v[44:47], v124 offset:48128
	v_exp_f32_e32 v72, v72
	v_exp_f32_e32 v73, v73
	v_exp_f32_e32 v74, v74
	v_exp_f32_e32 v75, v75
	v_pk_add_f32 v[120:121], v[120:121], v[68:69]
	v_pk_add_f32 v[122:123], v[122:123], v[70:71]
	s_waitcnt lgkmcnt(6)
	s_nop 0
	v_mfma_f32_32x32x64_f8f6f4 v[48:63], v[0:5], v[96:101], 0 cbsz:2 blgp:2
	ds_read_b128 v[0:3], v124 offset:49152
	v_exp_f32_e32 v76, v76
	v_exp_f32_e32 v77, v77
	v_exp_f32_e32 v78, v78
	v_exp_f32_e32 v79, v79
	v_pk_add_f32 v[120:121], v[120:121], v[72:73]
	v_pk_add_f32 v[122:123], v[122:123], v[74:75]
	v_mfma_f32_32x32x64_f8f6f4 v[48:63], v[6:11], v[102:107], v[48:63] cbsz:2 blgp:2
	ds_read_b128 v[4:7], v124 offset:50176
	ds_read_b128 v[8:11], v124 offset:51200
	v_exp_f32_e32 v80, v80
	v_exp_f32_e32 v81, v81
	v_exp_f32_e32 v82, v82
	v_exp_f32_e32 v83, v83
	v_pk_add_f32 v[120:121], v[120:121], v[76:77]
	v_pk_add_f32 v[122:123], v[122:123], v[78:79]
	v_mfma_f32_32x32x64_f8f6f4 v[48:63], v[12:17], v[108:113], v[48:63] cbsz:2 blgp:2
	ds_read_b128 v[12:15], v124 offset:52224
	v_exp_f32_e32 v84, v84
	v_exp_f32_e32 v85, v85
	v_exp_f32_e32 v86, v86
	v_exp_f32_e32 v87, v87
	v_pk_add_f32 v[120:121], v[120:121], v[80:81]
	v_pk_add_f32 v[122:123], v[122:123], v[82:83]
	v_mfma_f32_32x32x64_f8f6f4 v[48:63], v[18:23], v[114:119], v[48:63] cbsz:2 blgp:2
	ds_read_b128 v[16:19], v124 offset:53248
	ds_read_b128 v[20:23], v124 offset:54272
	v_exp_f32_e32 v88, v88
	v_exp_f32_e32 v89, v89
	v_exp_f32_e32 v90, v90
	v_exp_f32_e32 v91, v91
	v_pk_add_f32 v[120:121], v[120:121], v[84:85]
	v_pk_add_f32 v[122:123], v[122:123], v[86:87]
	s_waitcnt lgkmcnt(6)
	s_nop 0
	v_mfma_f32_32x32x64_f8f6f4 v[64:79], v[24:29], v[96:101], 0 cbsz:2 blgp:2
	ds_read_b128 v[24:27], v124 offset:55296
	v_exp_f32_e32 v92, v92
	v_exp_f32_e32 v93, v93
	v_exp_f32_e32 v94, v94
	v_exp_f32_e32 v95, v95
	v_pk_add_f32 v[120:121], v[120:121], v[88:89]
	v_pk_add_f32 v[122:123], v[122:123], v[90:91]
	v_mfma_f32_32x32x64_f8f6f4 v[64:79], v[30:35], v[102:107], v[64:79] cbsz:2 blgp:2
	ds_read_b128 v[28:31], v124 offset:56320
	ds_read_b128 v[32:35], v124 offset:57344
	v_exp_f32_e32 v48, v48
	v_exp_f32_e32 v49, v49
	v_exp_f32_e32 v50, v50
	v_exp_f32_e32 v51, v51
	v_pk_add_f32 v[120:121], v[120:121], v[92:93]
	v_pk_add_f32 v[122:123], v[122:123], v[94:95]
	v_mfma_f32_32x32x64_f8f6f4 v[64:79], v[36:41], v[108:113], v[64:79] cbsz:2 blgp:2
	ds_read_b128 v[36:39], v124 offset:58368
	v_exp_f32_e32 v52, v52
	v_exp_f32_e32 v53, v53
	v_exp_f32_e32 v54, v54
	v_exp_f32_e32 v55, v55
	v_pk_add_f32 v[120:121], v[120:121], v[48:49]
	v_pk_add_f32 v[122:123], v[122:123], v[50:51]
	v_mfma_f32_32x32x64_f8f6f4 v[64:79], v[42:47], v[114:119], v[64:79] cbsz:2 blgp:2
	ds_read_b128 v[40:43], v124 offset:59392
	ds_read_b128 v[44:47], v124 offset:60416
	v_exp_f32_e32 v56, v56
	v_exp_f32_e32 v57, v57
	v_exp_f32_e32 v58, v58
	v_exp_f32_e32 v59, v59
	v_pk_add_f32 v[120:121], v[120:121], v[52:53]
	v_pk_add_f32 v[122:123], v[122:123], v[54:55]
	s_setprio 0
	s_waitcnt vmcnt(0) lgkmcnt(6)
	s_barrier
	s_nop 0
	v_mfma_f32_32x32x64_f8f6f4 v[80:95], v[0:5], v[96:101], 0 cbsz:2 blgp:2
	ds_read_b128 v[0:3], v124
	v_exp_f32_e32 v60, v60
	v_exp_f32_e32 v61, v61
	v_exp_f32_e32 v62, v62
	v_exp_f32_e32 v63, v63
	v_pk_add_f32 v[120:121], v[120:121], v[56:57]
	v_pk_add_f32 v[122:123], v[122:123], v[58:59]
	v_mfma_f32_32x32x64_f8f6f4 v[80:95], v[6:11], v[102:107], v[80:95] cbsz:2 blgp:2
	ds_read_b128 v[4:7], v124 offset:1024
	ds_read_b128 v[8:11], v124 offset:2048
	v_exp_f32_e32 v64, v64
	v_exp_f32_e32 v65, v65
	v_exp_f32_e32 v66, v66
	v_exp_f32_e32 v67, v67
	v_pk_add_f32 v[120:121], v[120:121], v[60:61]
	v_pk_add_f32 v[122:123], v[122:123], v[62:63]
	v_mfma_f32_32x32x64_f8f6f4 v[80:95], v[12:17], v[108:113], v[80:95] cbsz:2 blgp:2
	ds_read_b128 v[12:15], v124 offset:3072
	v_exp_f32_e32 v68, v68
	v_exp_f32_e32 v69, v69
	v_exp_f32_e32 v70, v70
	v_exp_f32_e32 v71, v71
	v_pk_add_f32 v[120:121], v[120:121], v[64:65]
	v_pk_add_f32 v[122:123], v[122:123], v[66:67]
	v_mfma_f32_32x32x64_f8f6f4 v[80:95], v[18:23], v[114:119], v[80:95] cbsz:2 blgp:2
	ds_read_b128 v[16:19], v124 offset:4096
	ds_read_b128 v[20:23], v124 offset:5120
	v_exp_f32_e32 v72, v72
	v_exp_f32_e32 v73, v73
	v_exp_f32_e32 v74, v74
	v_exp_f32_e32 v75, v75
	v_pk_add_f32 v[120:121], v[120:121], v[68:69]
	v_pk_add_f32 v[122:123], v[122:123], v[70:71]
	s_waitcnt lgkmcnt(6)
	s_nop 0
	v_mfma_f32_32x32x64_f8f6f4 v[48:63], v[24:29], v[96:101], 0 cbsz:2 blgp:2
	ds_read_b128 v[24:27], v124 offset:6144
	v_exp_f32_e32 v76, v76
	v_exp_f32_e32 v77, v77
	v_exp_f32_e32 v78, v78
	v_exp_f32_e32 v79, v79
	v_pk_add_f32 v[120:121], v[120:121], v[72:73]
	v_pk_add_f32 v[122:123], v[122:123], v[74:75]
	v_mfma_f32_32x32x64_f8f6f4 v[48:63], v[30:35], v[102:107], v[48:63] cbsz:2 blgp:2
	ds_read_b128 v[28:31], v124 offset:7168
	ds_read_b128 v[32:35], v124 offset:8192
	v_exp_f32_e32 v80, v80
	v_exp_f32_e32 v81, v81
	v_exp_f32_e32 v82, v82
	v_exp_f32_e32 v83, v83
	v_pk_add_f32 v[120:121], v[120:121], v[76:77]
	v_pk_add_f32 v[122:123], v[122:123], v[78:79]
	s_cmp_lg_u32 s8, 10
	s_cbranch_scc1 .Lmk_nosplit_a
	v_add_f32_e32 v127, v120, v121
	v_add_f32_e32 v126, v122, v123
	v_mov_b32_e32 v120, 0
	v_mov_b32_e32 v121, 0
	v_mov_b32_e32 v122, 0
	v_mov_b32_e32 v123, 0
	v_add_f32_e32 v127, v127, v126
.Lmk_nosplit_a:
	s_nop 0
	v_mfma_f32_32x32x64_f8f6f4 v[48:63], v[36:41], v[108:113], v[48:63] cbsz:2 blgp:2
	ds_read_b128 v[36:39], v124 offset:9216
	v_exp_f32_e32 v84, v84
	v_exp_f32_e32 v85, v85
	v_exp_f32_e32 v86, v86
	v_exp_f32_e32 v87, v87
	v_pk_add_f32 v[120:121], v[120:121], v[80:81]
	v_pk_add_f32 v[122:123], v[122:123], v[82:83]
	v_mfma_f32_32x32x64_f8f6f4 v[48:63], v[42:47], v[114:119], v[48:63] cbsz:2 blgp:2
	ds_read_b128 v[40:43], v124 offset:10240
	ds_read_b128 v[44:47], v124 offset:11264
	v_exp_f32_e32 v88, v88
	v_exp_f32_e32 v89, v89
	v_exp_f32_e32 v90, v90
	v_exp_f32_e32 v91, v91
	v_pk_add_f32 v[120:121], v[120:121], v[84:85]
	v_pk_add_f32 v[122:123], v[122:123], v[86:87]
	s_waitcnt lgkmcnt(6)
	s_nop 0
	v_mfma_f32_32x32x64_f8f6f4 v[64:79], v[0:5], v[96:101], 0 cbsz:2 blgp:2
	v_exp_f32_e32 v92, v92
	v_exp_f32_e32 v93, v93
	v_exp_f32_e32 v94, v94
	v_exp_f32_e32 v95, v95
	v_pk_add_f32 v[120:121], v[120:121], v[88:89]
	v_pk_add_f32 v[122:123], v[122:123], v[90:91]
	v_mfma_f32_32x32x64_f8f6f4 v[64:79], v[6:11], v[102:107], v[64:79] cbsz:2 blgp:2
	v_exp_f32_e32 v48, v48
	v_exp_f32_e32 v49, v49
	v_exp_f32_e32 v50, v50
	v_exp_f32_e32 v51, v51
	v_pk_add_f32 v[120:121], v[120:121], v[92:93]
	v_pk_add_f32 v[122:123], v[122:123], v[94:95]
	v_mfma_f32_32x32x64_f8f6f4 v[64:79], v[12:17], v[108:113], v[64:79] cbsz:2 blgp:2
	v_exp_f32_e32 v52, v52
	v_exp_f32_e32 v53, v53
	v_exp_f32_e32 v54, v54
	v_exp_f32_e32 v55, v55
	v_pk_add_f32 v[120:121], v[120:121], v[48:49]
	v_pk_add_f32 v[122:123], v[122:123], v[50:51]
	v_mfma_f32_32x32x64_f8f6f4 v[64:79], v[18:23], v[114:119], v[64:79] cbsz:2 blgp:2
	v_exp_f32_e32 v56, v56
	v_exp_f32_e32 v57, v57
	v_exp_f32_e32 v58, v58
	v_exp_f32_e32 v59, v59
	v_pk_add_f32 v[120:121], v[120:121], v[52:53]
	v_pk_add_f32 v[122:123], v[122:123], v[54:55]
	s_waitcnt lgkmcnt(0)
	s_nop 0
	v_mfma_f32_32x32x64_f8f6f4 v[80:95], v[24:29], v[96:101], 0 cbsz:2 blgp:2
	v_exp_f32_e32 v60, v60
	v_exp_f32_e32 v61, v61
	v_exp_f32_e32 v62, v62
	v_exp_f32_e32 v63, v63
	v_pk_add_f32 v[120:121], v[120:121], v[56:57]
	v_pk_add_f32 v[122:123], v[122:123], v[58:59]
	v_mfma_f32_32x32x64_f8f6f4 v[80:95], v[30:35], v[102:107], v[80:95] cbsz:2 blgp:2
	v_exp_f32_e32 v64, v64
	v_exp_f32_e32 v65, v65
	v_exp_f32_e32 v66, v66
	v_exp_f32_e32 v67, v67
	v_pk_add_f32 v[120:121], v[120:121], v[60:61]
	v_pk_add_f32 v[122:123], v[122:123], v[62:63]
	v_mfma_f32_32x32x64_f8f6f4 v[80:95], v[36:41], v[108:113], v[80:95] cbsz:2 blgp:2
	v_exp_f32_e32 v68, v68
	v_exp_f32_e32 v69, v69
	v_exp_f32_e32 v70, v70
	v_exp_f32_e32 v71, v71
	v_pk_add_f32 v[120:121], v[120:121], v[64:65]
	v_pk_add_f32 v[122:123], v[122:123], v[66:67]
	v_mfma_f32_32x32x64_f8f6f4 v[80:95], v[42:47], v[114:119], v[80:95] cbsz:2 blgp:2
	v_exp_f32_e32 v72, v72
	v_exp_f32_e32 v73, v73
	v_exp_f32_e32 v74, v74
	v_exp_f32_e32 v75, v75
	v_pk_add_f32 v[120:121], v[120:121], v[68:69]
	v_pk_add_f32 v[122:123], v[122:123], v[70:71]
	v_exp_f32_e32 v76, v76
	v_exp_f32_e32 v77, v77
	v_exp_f32_e32 v78, v78
	v_exp_f32_e32 v79, v79
	v_pk_add_f32 v[120:121], v[120:121], v[72:73]
	v_pk_add_f32 v[122:123], v[122:123], v[74:75]
	s_nop 1
	v_exp_f32_e32 v80, v80
	v_exp_f32_e32 v81, v81
	v_exp_f32_e32 v82, v82
	v_exp_f32_e32 v83, v83
	v_pk_add_f32 v[120:121], v[120:121], v[76:77]
	v_pk_add_f32 v[122:123], v[122:123], v[78:79]
	v_exp_f32_e32 v84, v84
	v_exp_f32_e32 v85, v85
	v_exp_f32_e32 v86, v86
	v_exp_f32_e32 v87, v87
	v_pk_add_f32 v[120:121], v[120:121], v[80:81]
	v_pk_add_f32 v[122:123], v[122:123], v[82:83]
	v_exp_f32_e32 v88, v88
	v_exp_f32_e32 v89, v89
	v_exp_f32_e32 v90, v90
	v_exp_f32_e32 v91, v91
	v_pk_add_f32 v[120:121], v[120:121], v[84:85]
	v_pk_add_f32 v[122:123], v[122:123], v[86:87]
	v_exp_f32_e32 v92, v92
	v_exp_f32_e32 v93, v93
	v_exp_f32_e32 v94, v94
	v_exp_f32_e32 v95, v95
	v_pk_add_f32 v[120:121], v[120:121], v[88:89]
	v_pk_add_f32 v[122:123], v[122:123], v[90:91]
	v_pk_add_f32 v[120:121], v[120:121], v[92:93]
	v_pk_add_f32 v[122:123], v[122:123], v[94:95]
	v_add_f32_e32 v120, v120, v121
	v_add_f32_e32 v122, v122, v123
	v_lshrrev_b32_e32 v126, 2, v124
	v_add_f32_e32 v120, v120, v122
	v_mov_b32_e32 v123, v127
	v_mov_b32_e32 v122, v120
	s_mov_b64 s[4:5], s[30:31]
	s_mov_b64 s[6:7], s[32:33]
	s_lshl_b32 s14, s14, 7
	v_add_u32_e32 v126, s14, v126
	s_nop 1
	v_permlane32_swap_b32_e32 v120, v122
	v_permlane32_swap_b32_e32 v127, v123
	s_nop 1
	v_add_f32_e32 v120, v120, v122
	v_add_f32_e32 v127, v127, v123
	v_cmp_gt_u32_e32 vcc, 0x200, v124
	s_and_saveexec_b64 s[16:17], vcc
	s_cbranch_execz .Lmk_end_a
	s_cmp_lt_u32 s8, 10
	s_cbranch_scc1 .Lmk_pos_only_a
	s_cmp_eq_u32 s8, 10
	s_cbranch_scc0 .Lmk_neg_only_a
	global_atomic_add_f32 v126, v127, s[4:5]

.Lmk_vb:
	s_mov_b32 m0, s13
	s_nop 0
	global_load_lds_dwordx4 v124, s[10:11]
	global_load_dwordx4 v[96:99], v124, s[18:19]
	global_load_dwordx4 v[100:103], v124, s[18:19] offset:1024
	global_load_dwordx4 v[104:107], v124, s[18:19] offset:2048
	global_load_dwordx4 v[108:111], v124, s[22:23]
	global_load_dwordx4 v[112:115], v124, s[22:23] offset:1024
	global_load_dwordx4 v[116:119], v124, s[22:23] offset:2048
	s_add_u32 s24, s10, 0x3000
	s_addc_u32 s25, s11, 0
	s_add_u32 s26, s13, 0x3000
	s_mov_b32 m0, s26
	s_nop 0
	global_load_lds_dwordx4 v124, s[24:25]
	s_add_u32 s24, s10, 0x6000
	s_addc_u32 s25, s11, 0
	s_add_u32 s26, s13, 0x6000
	s_mov_b32 m0, s26
	s_nop 0
	global_load_lds_dwordx4 v124, s[24:25]
	s_add_u32 s24, s10, 0x9000
	s_addc_u32 s25, s11, 0
	s_add_u32 s26, s13, 0x9000
	s_mov_b32 m0, s26
	s_nop 0
	global_load_lds_dwordx4 v124, s[24:25]
	s_add_u32 s24, s10, 0xc000
	s_addc_u32 s25, s11, 0
	s_add_u32 s26, s13, 0xc000
	s_mov_b32 m0, s26
	s_nop 0
	global_load_lds_dwordx4 v124, s[24:25]
	s_waitcnt vmcnt(4)
	s_barrier
	ds_read_b128 v[0:3], v124
	ds_read_b128 v[4:7], v124 offset:1024
	ds_read_b128 v[8:11], v124 offset:2048
	ds_read_b128 v[12:15], v124 offset:3072
	ds_read_b128 v[16:19], v124 offset:4096
	ds_read_b128 v[20:23], v124 offset:5120
	s_waitcnt lgkmcnt(0)
	s_setprio 3
	s_nop 0
	v_mfma_f32_32x32x64_f8f6f4 v[48:63], v[0:5], v[96:101], 0 cbsz:2 blgp:2
	ds_read_b128 v[24:27], v124 offset:6144
	v_mfma_f32_32x32x64_f8f6f4 v[48:63], v[6:11], v[102:107], v[48:63] cbsz:2 blgp:2
	ds_read_b128 v[28:31], v124 offset:7168
	ds_read_b128 v[32:35], v124 offset:8192
	v_mfma_f32_32x32x64_f8f6f4 v[48:63], v[12:17], v[108:113], v[48:63] cbsz:2 blgp:2
	ds_read_b128 v[36:39], v124 offset:9216
	v_mfma_f32_32x32x64_f8f6f4 v[48:63], v[18:23], v[114:119], v[48:63] cbsz:2 blgp:2
	ds_read_b128 v[40:43], v124 offset:10240
	ds_read_b128 v[44:47], v124 offset:11264
	s_waitcnt vmcnt(0) lgkmcnt(0)
	s_barrier
	s_add_u32 s24, s10, 0xf000
	s_addc_u32 s25, s11, 0
	s_mov_b32 m0, s13
	s_nop 0
	global_load_lds_dwordx4 v124, s[24:25]
	s_nop 0
	v_mfma_f32_32x32x64_f8f6f4 v[64:79], v[24:29], v[96:101], 0 cbsz:2 blgp:2
	ds_read_b128 v[0:3], v124 offset:12288
	ds_read_b128 v[4:7], v124 offset:13312
	ds_read_b128 v[8:11], v124 offset:14336
	ds_read_b128 v[24:27], v124 offset:18432
	v_mfma_f32_32x32x64_f8f6f4 v[64:79], v[30:35], v[102:107], v[64:79] cbsz:2 blgp:2
	ds_read_b128 v[12:15], v124 offset:15360
	ds_read_b128 v[16:19], v124 offset:16384
	ds_read_b128 v[20:23], v124 offset:17408
	ds_read_b128 v[28:31], v124 offset:19456
	ds_read_b128 v[32:35], v124 offset:20480
	v_exp_f32_e32 v48, v48
	v_exp_f32_e32 v49, v49
	v_exp_f32_e32 v50, v50
	v_exp_f32_e32 v51, v51
	v_mfma_f32_32x32x64_f8f6f4 v[64:79], v[36:41], v[108:113], v[64:79] cbsz:2 blgp:2
	ds_read_b128 v[36:39], v124 offset:21504
	v_exp_f32_e32 v52, v52
	v_exp_f32_e32 v53, v53
	v_exp_f32_e32 v54, v54
	v_exp_f32_e32 v55, v55
	v_pk_add_f32 v[120:121], v[120:121], v[48:49]
	v_pk_add_f32 v[122:123], v[122:123], v[50:51]
	v_mfma_f32_32x32x64_f8f6f4 v[64:79], v[42:47], v[114:119], v[64:79] cbsz:2 blgp:2
	ds_read_b128 v[40:43], v124 offset:22528
	ds_read_b128 v[44:47], v124 offset:23552
	v_exp_f32_e32 v56, v56
	v_exp_f32_e32 v57, v57
	v_exp_f32_e32 v58, v58
	v_exp_f32_e32 v59, v59
	v_pk_add_f32 v[120:121], v[120:121], v[52:53]
	v_pk_add_f32 v[122:123], v[122:123], v[54:55]
	s_waitcnt lgkmcnt(5)
	s_nop 0
	v_mfma_f32_32x32x64_f8f6f4 v[80:95], v[0:5], v[96:101], 0 cbsz:2 blgp:2
	ds_read_b128 v[0:3], v124 offset:24576
	v_exp_f32_e32 v60, v60
	v_exp_f32_e32 v61, v61
	v_exp_f32_e32 v62, v62
	v_exp_f32_e32 v63, v63
	v_pk_add_f32 v[120:121], v[120:121], v[56:57]
	v_pk_add_f32 v[122:123], v[122:123], v[58:59]
	v_mfma_f32_32x32x64_f8f6f4 v[80:95], v[6:11], v[102:107], v[80:95] cbsz:2 blgp:2
	ds_read_b128 v[4:7], v124 offset:25600
	ds_read_b128 v[8:11], v124 offset:26624
	v_exp_f32_e32 v64, v64
	v_exp_f32_e32 v65, v65
	v_exp_f32_e32 v66, v66
	v_exp_f32_e32 v67, v67
	v_pk_add_f32 v[120:121], v[120:121], v[60:61]
	v_pk_add_f32 v[122:123], v[122:123], v[62:63]
	v_mfma_f32_32x32x64_f8f6f4 v[80:95], v[12:17], v[108:113], v[80:95] cbsz:2 blgp:2
	ds_read_b128 v[12:15], v124 offset:27648
	v_exp_f32_e32 v68, v68
	v_exp_f32_e32 v69, v69
	v_exp_f32_e32 v70, v70
	v_exp_f32_e32 v71, v71
	v_pk_add_f32 v[120:121], v[120:121], v[64:65]
	v_pk_add_f32 v[122:123], v[122:123], v[66:67]
	v_mfma_f32_32x32x64_f8f6f4 v[80:95], v[18:23], v[114:119], v[80:95] cbsz:2 blgp:2
	ds_read_b128 v[16:19], v124 offset:28672
	ds_read_b128 v[20:23], v124 offset:29696
	v_exp_f32_e32 v72, v72
	v_exp_f32_e32 v73, v73
	v_exp_f32_e32 v74, v74
	v_exp_f32_e32 v75, v75
	v_pk_add_f32 v[120:121], v[120:121], v[68:69]
	v_pk_add_f32 v[122:123], v[122:123], v[70:71]
	s_waitcnt lgkmcnt(6)
	s_nop 0
	v_mfma_f32_32x32x64_f8f6f4 v[48:63], v[24:29], v[96:101], 0 cbsz:2 blgp:2
	ds_read_b128 v[24:27], v124 offset:30720
	v_exp_f32_e32 v76, v76
	v_exp_f32_e32 v77, v77
	v_exp_f32_e32 v78, v78
	v_exp_f32_e32 v79, v79
	v_pk_add_f32 v[120:121], v[120:121], v[72:73]
	v_pk_add_f32 v[122:123], v[122:123], v[74:75]
	v_mfma_f32_32x32x64_f8f6f4 v[48:63], v[30:35], v[102:107], v[48:63] cbsz:2 blgp:2
	ds_read_b128 v[28:31], v124 offset:31744
	ds_read_b128 v[32:35], v124 offset:32768
	v_exp_f32_e32 v80, v80
	v_exp_f32_e32 v81, v81
	v_exp_f32_e32 v82, v82
	v_exp_f32_e32 v83, v83
	v_pk_add_f32 v[120:121], v[120:121], v[76:77]
	v_pk_add_f32 v[122:123], v[122:123], v[78:79]
	v_mfma_f32_32x32x64_f8f6f4 v[48:63], v[36:41], v[108:113], v[48:63] cbsz:2 blgp:2
	ds_read_b128 v[36:39], v124 offset:33792
	v_exp_f32_e32 v84, v84
	v_exp_f32_e32 v85, v85
	v_exp_f32_e32 v86, v86
	v_exp_f32_e32 v87, v87
	v_pk_add_f32 v[120:121], v[120:121], v[80:81]
	v_pk_add_f32 v[122:123], v[122:123], v[82:83]
	v_mfma_f32_32x32x64_f8f6f4 v[48:63], v[42:47], v[114:119], v[48:63] cbsz:2 blgp:2
	ds_read_b128 v[40:43], v124 offset:34816
	ds_read_b128 v[44:47], v124 offset:35840
	v_exp_f32_e32 v88, v88
	v_exp_f32_e32 v89, v89
	v_exp_f32_e32 v90, v90
	v_exp_f32_e32 v91, v91
	v_pk_add_f32 v[120:121], v[120:121], v[84:85]
	v_pk_add_f32 v[122:123], v[122:123], v[86:87]
	s_setprio 2
	s_waitcnt lgkmcnt(6)
	v_mfma_f32_32x32x64_f8f6f4 v[64:79], v[0:5], v[96:101], 0 cbsz:2 blgp:2
	ds_read_b128 v[0:3], v124 offset:36864
	v_exp_f32_e32 v92, v92
	v_exp_f32_e32 v93, v93
	v_exp_f32_e32 v94, v94
	v_exp_f32_e32 v95, v95
	v_pk_add_f32 v[120:121], v[120:121], v[88:89]
	v_pk_add_f32 v[122:123], v[122:123], v[90:91]
	v_mfma_f32_32x32x64_f8f6f4 v[64:79], v[6:11], v[102:107], v[64:79] cbsz:2 blgp:2
	ds_read_b128 v[4:7], v124 offset:37888
	ds_read_b128 v[8:11], v124 offset:38912
	v_exp_f32_e32 v48, v48
	v_exp_f32_e32 v49, v49
	v_exp_f32_e32 v50, v50
	v_exp_f32_e32 v51, v51
	v_pk_add_f32 v[120:121], v[120:121], v[92:93]
	v_pk_add_f32 v[122:123], v[122:123], v[94:95]
	v_mfma_f32_32x32x64_f8f6f4 v[64:79], v[12:17], v[108:113], v[64:79] cbsz:2 blgp:2
	ds_read_b128 v[12:15], v124 offset:39936
	v_exp_f32_e32 v52, v52
	v_exp_f32_e32 v53, v53
	v_exp_f32_e32 v54, v54
	v_exp_f32_e32 v55, v55
	v_pk_add_f32 v[120:121], v[120:121], v[48:49]
	v_pk_add_f32 v[122:123], v[122:123], v[50:51]
	v_mfma_f32_32x32x64_f8f6f4 v[64:79], v[18:23], v[114:119], v[64:79] cbsz:2 blgp:2
	ds_read_b128 v[16:19], v124 offset:40960
	ds_read_b128 v[20:23], v124 offset:41984
	v_exp_f32_e32 v56, v56
	v_exp_f32_e32 v57, v57
	v_exp_f32_e32 v58, v58
	v_exp_f32_e32 v59, v59
	v_pk_add_f32 v[120:121], v[120:121], v[52:53]
	v_pk_add_f32 v[122:123], v[122:123], v[54:55]
	s_waitcnt lgkmcnt(6)
	s_nop 0
	v_mfma_f32_32x32x64_f8f6f4 v[80:95], v[24:29], v[96:101], 0 cbsz:2 blgp:2
	ds_read_b128 v[24:27], v124 offset:43008
	v_exp_f32_e32 v60, v60
	v_exp_f32_e32 v61, v61
	v_exp_f32_e32 v62, v62
	v_exp_f32_e32 v63, v63
	v_pk_add_f32 v[120:121], v[120:121], v[56:57]
	v_pk_add_f32 v[122:123], v[122:123], v[58:59]
	v_mfma_f32_32x32x64_f8f6f4 v[80:95], v[30:35], v[102:107], v[80:95] cbsz:2 blgp:2
	ds_read_b128 v[28:31], v124 offset:44032
	ds_read_b128 v[32:35], v124 offset:45056
	v_exp_f32_e32 v64, v64
	v_exp_f32_e32 v65, v65
	v_exp_f32_e32 v66, v66
	v_exp_f32_e32 v67, v67
	v_pk_add_f32 v[120:121], v[120:121], v[60:61]
	v_pk_add_f32 v[122:123], v[122:123], v[62:63]
	v_mfma_f32_32x32x64_f8f6f4 v[80:95], v[36:41], v[108:113], v[80:95] cbsz:2 blgp:2
	ds_read_b128 v[36:39], v124 offset:46080
	v_exp_f32_e32 v68, v68
	v_exp_f32_e32 v69, v69
	v_exp_f32_e32 v70, v70
	v_exp_f32_e32 v71, v71
	v_pk_add_f32 v[120:121], v[120:121], v[64:65]
	v_pk_add_f32 v[122:123], v[122:123], v[66:67]
	v_mfma_f32_32x32x64_f8f6f4 v[80:95], v[42:47], v[114:119], v[80:95] cbsz:2 blgp:2
	ds_read_b128 v[40:43], v124 offset:47104
	ds_read_b128 v[44:47], v124 offset:48128
	v_exp_f32_e32 v72, v72
	v_exp_f32_e32 v73, v73
	v_exp_f32_e32 v74, v74
	v_exp_f32_e32 v75, v75
	v_pk_add_f32 v[120:121], v[120:121], v[68:69]
	v_pk_add_f32 v[122:123], v[122:123], v[70:71]
	s_waitcnt lgkmcnt(6)
	s_nop 0
	v_mfma_f32_32x32x64_f8f6f4 v[48:63], v[0:5], v[96:101], 0 cbsz:2 blgp:2
	ds_read_b128 v[0:3], v124 offset:49152
	v_exp_f32_e32 v76, v76
	v_exp_f32_e32 v77, v77
	v_exp_f32_e32 v78, v78
	v_exp_f32_e32 v79, v79
	v_pk_add_f32 v[120:121], v[120:121], v[72:73]
	v_pk_add_f32 v[122:123], v[122:123], v[74:75]
	v_mfma_f32_32x32x64_f8f6f4 v[48:63], v[6:11], v[102:107], v[48:63] cbsz:2 blgp:2
	ds_read_b128 v[4:7], v124 offset:50176
	ds_read_b128 v[8:11], v124 offset:51200
	v_exp_f32_e32 v80, v80
	v_exp_f32_e32 v81, v81
	v_exp_f32_e32 v82, v82
	v_exp_f32_e32 v83, v83
	v_pk_add_f32 v[120:121], v[120:121], v[76:77]
	v_pk_add_f32 v[122:123], v[122:123], v[78:79]
	v_mfma_f32_32x32x64_f8f6f4 v[48:63], v[12:17], v[108:113], v[48:63] cbsz:2 blgp:2
	ds_read_b128 v[12:15], v124 offset:52224
	v_exp_f32_e32 v84, v84
	v_exp_f32_e32 v85, v85
	v_exp_f32_e32 v86, v86
	v_exp_f32_e32 v87, v87
	v_pk_add_f32 v[120:121], v[120:121], v[80:81]
	v_pk_add_f32 v[122:123], v[122:123], v[82:83]
	v_mfma_f32_32x32x64_f8f6f4 v[48:63], v[18:23], v[114:119], v[48:63] cbsz:2 blgp:2
	ds_read_b128 v[16:19], v124 offset:53248
	ds_read_b128 v[20:23], v124 offset:54272
	v_exp_f32_e32 v88, v88
	v_exp_f32_e32 v89, v89
	v_exp_f32_e32 v90, v90
	v_exp_f32_e32 v91, v91
	v_pk_add_f32 v[120:121], v[120:121], v[84:85]
	v_pk_add_f32 v[122:123], v[122:123], v[86:87]
	s_waitcnt lgkmcnt(6)
	s_nop 0
	v_mfma_f32_32x32x64_f8f6f4 v[64:79], v[24:29], v[96:101], 0 cbsz:2 blgp:2
	ds_read_b128 v[24:27], v124 offset:55296
	v_exp_f32_e32 v92, v92
	v_exp_f32_e32 v93, v93
	v_exp_f32_e32 v94, v94
	v_exp_f32_e32 v95, v95
	v_pk_add_f32 v[120:121], v[120:121], v[88:89]
	v_pk_add_f32 v[122:123], v[122:123], v[90:91]
	v_mfma_f32_32x32x64_f8f6f4 v[64:79], v[30:35], v[102:107], v[64:79] cbsz:2 blgp:2
	ds_read_b128 v[28:31], v124 offset:56320
	ds_read_b128 v[32:35], v124 offset:57344
	v_exp_f32_e32 v48, v48
	v_exp_f32_e32 v49, v49
	v_exp_f32_e32 v50, v50
	v_exp_f32_e32 v51, v51
	v_pk_add_f32 v[120:121], v[120:121], v[92:93]
	v_pk_add_f32 v[122:123], v[122:123], v[94:95]
	v_mfma_f32_32x32x64_f8f6f4 v[64:79], v[36:41], v[108:113], v[64:79] cbsz:2 blgp:2
	ds_read_b128 v[36:39], v124 offset:58368
	v_exp_f32_e32 v52, v52
	v_exp_f32_e32 v53, v53
	v_exp_f32_e32 v54, v54
	v_exp_f32_e32 v55, v55
	v_pk_add_f32 v[120:121], v[120:121], v[48:49]
	v_pk_add_f32 v[122:123], v[122:123], v[50:51]
	v_mfma_f32_32x32x64_f8f6f4 v[64:79], v[42:47], v[114:119], v[64:79] cbsz:2 blgp:2
	ds_read_b128 v[40:43], v124 offset:59392
	ds_read_b128 v[44:47], v124 offset:60416
	v_exp_f32_e32 v56, v56
	v_exp_f32_e32 v57, v57
	v_exp_f32_e32 v58, v58
	v_exp_f32_e32 v59, v59
	v_pk_add_f32 v[120:121], v[120:121], v[52:53]
	v_pk_add_f32 v[122:123], v[122:123], v[54:55]
	s_setprio 1
	s_waitcnt vmcnt(0) lgkmcnt(6)
	s_barrier
	s_nop 0
	v_mfma_f32_32x32x64_f8f6f4 v[80:95], v[0:5], v[96:101], 0 cbsz:2 blgp:2
	ds_read_b128 v[0:3], v124
	v_exp_f32_e32 v60, v60
	v_exp_f32_e32 v61, v61
	v_exp_f32_e32 v62, v62
	v_exp_f32_e32 v63, v63
	v_pk_add_f32 v[120:121], v[120:121], v[56:57]
	v_pk_add_f32 v[122:123], v[122:123], v[58:59]
	v_mfma_f32_32x32x64_f8f6f4 v[80:95], v[6:11], v[102:107], v[80:95] cbsz:2 blgp:2
	ds_read_b128 v[4:7], v124 offset:1024
	ds_read_b128 v[8:11], v124 offset:2048
	v_exp_f32_e32 v64, v64
	v_exp_f32_e32 v65, v65
	v_exp_f32_e32 v66, v66
	v_exp_f32_e32 v67, v67
	v_pk_add_f32 v[120:121], v[120:121], v[60:61]
	v_pk_add_f32 v[122:123], v[122:123], v[62:63]
	v_mfma_f32_32x32x64_f8f6f4 v[80:95], v[12:17], v[108:113], v[80:95] cbsz:2 blgp:2
	ds_read_b128 v[12:15], v124 offset:3072
	v_exp_f32_e32 v68, v68
	v_exp_f32_e32 v69, v69
	v_exp_f32_e32 v70, v70
	v_exp_f32_e32 v71, v71
	v_pk_add_f32 v[120:121], v[120:121], v[64:65]
	v_pk_add_f32 v[122:123], v[122:123], v[66:67]
	v_mfma_f32_32x32x64_f8f6f4 v[80:95], v[18:23], v[114:119], v[80:95] cbsz:2 blgp:2
	ds_read_b128 v[16:19], v124 offset:4096
	ds_read_b128 v[20:23], v124 offset:5120
	v_exp_f32_e32 v72, v72
	v_exp_f32_e32 v73, v73
	v_exp_f32_e32 v74, v74
	v_exp_f32_e32 v75, v75
	v_pk_add_f32 v[120:121], v[120:121], v[68:69]
	v_pk_add_f32 v[122:123], v[122:123], v[70:71]
	s_waitcnt lgkmcnt(6)
	s_nop 0
	v_mfma_f32_32x32x64_f8f6f4 v[48:63], v[24:29], v[96:101], 0 cbsz:2 blgp:2
	ds_read_b128 v[24:27], v124 offset:6144
	v_exp_f32_e32 v76, v76
	v_exp_f32_e32 v77, v77
	v_exp_f32_e32 v78, v78
	v_exp_f32_e32 v79, v79
	v_pk_add_f32 v[120:121], v[120:121], v[72:73]
	v_pk_add_f32 v[122:123], v[122:123], v[74:75]
	v_mfma_f32_32x32x64_f8f6f4 v[48:63], v[30:35], v[102:107], v[48:63] cbsz:2 blgp:2
	ds_read_b128 v[28:31], v124 offset:7168
	ds_read_b128 v[32:35], v124 offset:8192
	v_exp_f32_e32 v80, v80
	v_exp_f32_e32 v81, v81
	v_exp_f32_e32 v82, v82
	v_exp_f32_e32 v83, v83
	v_pk_add_f32 v[120:121], v[120:121], v[76:77]
	v_pk_add_f32 v[122:123], v[122:123], v[78:79]
	s_cmp_lg_u32 s8, 10
	s_cbranch_scc1 .Lmk_nosplit_b
	v_add_f32_e32 v127, v120, v121
	v_add_f32_e32 v126, v122, v123
	v_mov_b32_e32 v120, 0
	v_mov_b32_e32 v121, 0
	v_mov_b32_e32 v122, 0
	v_mov_b32_e32 v123, 0
	v_add_f32_e32 v127, v127, v126
.Lmk_nosplit_b:
	s_nop 0
	v_mfma_f32_32x32x64_f8f6f4 v[48:63], v[36:41], v[108:113], v[48:63] cbsz:2 blgp:2
	ds_read_b128 v[36:39], v124 offset:9216
	v_exp_f32_e32 v84, v84
	v_exp_f32_e32 v85, v85
	v_exp_f32_e32 v86, v86
	v_exp_f32_e32 v87, v87
	v_pk_add_f32 v[120:121], v[120:121], v[80:81]
	v_pk_add_f32 v[122:123], v[122:123], v[82:83]
	v_mfma_f32_32x32x64_f8f6f4 v[48:63], v[42:47], v[114:119], v[48:63] cbsz:2 blgp:2
	ds_read_b128 v[40:43], v124 offset:10240
	ds_read_b128 v[44:47], v124 offset:11264
	v_exp_f32_e32 v88, v88
	v_exp_f32_e32 v89, v89
	v_exp_f32_e32 v90, v90
	v_exp_f32_e32 v91, v91
	v_pk_add_f32 v[120:121], v[120:121], v[84:85]
	v_pk_add_f32 v[122:123], v[122:123], v[86:87]
	s_setprio 0
	s_waitcnt lgkmcnt(6)
	v_mfma_f32_32x32x64_f8f6f4 v[64:79], v[0:5], v[96:101], 0 cbsz:2 blgp:2
	v_exp_f32_e32 v92, v92
	v_exp_f32_e32 v93, v93
	v_exp_f32_e32 v94, v94
	v_exp_f32_e32 v95, v95
	v_pk_add_f32 v[120:121], v[120:121], v[88:89]
	v_pk_add_f32 v[122:123], v[122:123], v[90:91]
	v_mfma_f32_32x32x64_f8f6f4 v[64:79], v[6:11], v[102:107], v[64:79] cbsz:2 blgp:2
	v_exp_f32_e32 v48, v48
	v_exp_f32_e32 v49, v49
	v_exp_f32_e32 v50, v50
	v_exp_f32_e32 v51, v51
	v_pk_add_f32 v[120:121], v[120:121], v[92:93]
	v_pk_add_f32 v[122:123], v[122:123], v[94:95]
	v_mfma_f32_32x32x64_f8f6f4 v[64:79], v[12:17], v[108:113], v[64:79] cbsz:2 blgp:2
	v_exp_f32_e32 v52, v52
	v_exp_f32_e32 v53, v53
	v_exp_f32_e32 v54, v54
	v_exp_f32_e32 v55, v55
	v_pk_add_f32 v[120:121], v[120:121], v[48:49]
	v_pk_add_f32 v[122:123], v[122:123], v[50:51]
	v_mfma_f32_32x32x64_f8f6f4 v[64:79], v[18:23], v[114:119], v[64:79] cbsz:2 blgp:2
	v_exp_f32_e32 v56, v56
	v_exp_f32_e32 v57, v57
	v_exp_f32_e32 v58, v58
	v_exp_f32_e32 v59, v59
	v_pk_add_f32 v[120:121], v[120:121], v[52:53]
	v_pk_add_f32 v[122:123], v[122:123], v[54:55]
	s_waitcnt lgkmcnt(0)
	s_nop 0
	v_mfma_f32_32x32x64_f8f6f4 v[80:95], v[24:29], v[96:101], 0 cbsz:2 blgp:2
	v_exp_f32_e32 v60, v60
	v_exp_f32_e32 v61, v61
	v_exp_f32_e32 v62, v62
	v_exp_f32_e32 v63, v63
	v_pk_add_f32 v[120:121], v[120:121], v[56:57]
	v_pk_add_f32 v[122:123], v[122:123], v[58:59]
	v_mfma_f32_32x32x64_f8f6f4 v[80:95], v[30:35], v[102:107], v[80:95] cbsz:2 blgp:2
	v_exp_f32_e32 v64, v64
	v_exp_f32_e32 v65, v65
	v_exp_f32_e32 v66, v66
	v_exp_f32_e32 v67, v67
	v_pk_add_f32 v[120:121], v[120:121], v[60:61]
	v_pk_add_f32 v[122:123], v[122:123], v[62:63]
	v_mfma_f32_32x32x64_f8f6f4 v[80:95], v[36:41], v[108:113], v[80:95] cbsz:2 blgp:2
	v_exp_f32_e32 v68, v68
	v_exp_f32_e32 v69, v69
	v_exp_f32_e32 v70, v70
	v_exp_f32_e32 v71, v71
	v_pk_add_f32 v[120:121], v[120:121], v[64:65]
	v_pk_add_f32 v[122:123], v[122:123], v[66:67]
	v_mfma_f32_32x32x64_f8f6f4 v[80:95], v[42:47], v[114:119], v[80:95] cbsz:2 blgp:2
	v_exp_f32_e32 v72, v72
	v_exp_f32_e32 v73, v73
	v_exp_f32_e32 v74, v74
	v_exp_f32_e32 v75, v75
	v_pk_add_f32 v[120:121], v[120:121], v[68:69]
	v_pk_add_f32 v[122:123], v[122:123], v[70:71]
	v_exp_f32_e32 v76, v76
	v_exp_f32_e32 v77, v77
	v_exp_f32_e32 v78, v78
	v_exp_f32_e32 v79, v79
	v_pk_add_f32 v[120:121], v[120:121], v[72:73]
	v_pk_add_f32 v[122:123], v[122:123], v[74:75]
	s_nop 1
	v_exp_f32_e32 v80, v80
	v_exp_f32_e32 v81, v81
	v_exp_f32_e32 v82, v82
	v_exp_f32_e32 v83, v83
	v_pk_add_f32 v[120:121], v[120:121], v[76:77]
	v_pk_add_f32 v[122:123], v[122:123], v[78:79]
	v_exp_f32_e32 v84, v84
	v_exp_f32_e32 v85, v85
	v_exp_f32_e32 v86, v86
	v_exp_f32_e32 v87, v87
	v_pk_add_f32 v[120:121], v[120:121], v[80:81]
	v_pk_add_f32 v[122:123], v[122:123], v[82:83]
	v_exp_f32_e32 v88, v88
	v_exp_f32_e32 v89, v89
	v_exp_f32_e32 v90, v90
	v_exp_f32_e32 v91, v91
	v_pk_add_f32 v[120:121], v[120:121], v[84:85]
	v_pk_add_f32 v[122:123], v[122:123], v[86:87]
	v_exp_f32_e32 v92, v92
	v_exp_f32_e32 v93, v93
	v_exp_f32_e32 v94, v94
	v_exp_f32_e32 v95, v95
	v_pk_add_f32 v[120:121], v[120:121], v[88:89]
	v_pk_add_f32 v[122:123], v[122:123], v[90:91]
	v_pk_add_f32 v[120:121], v[120:121], v[92:93]
	v_pk_add_f32 v[122:123], v[122:123], v[94:95]
	v_add_f32_e32 v120, v120, v121
	v_add_f32_e32 v122, v122, v123
	v_lshrrev_b32_e32 v126, 2, v124
	v_add_f32_e32 v120, v120, v122
	v_mov_b32_e32 v123, v127
	v_mov_b32_e32 v122, v120
	s_mov_b64 s[4:5], s[30:31]
	s_mov_b64 s[6:7], s[32:33]
	s_lshl_b32 s14, s14, 7
	v_add_u32_e32 v126, s14, v126
	s_nop 1
	v_permlane32_swap_b32_e32 v120, v122
	v_permlane32_swap_b32_e32 v127, v123
	s_nop 1
	v_add_f32_e32 v120, v120, v122
	v_add_f32_e32 v127, v127, v123
	v_cmp_gt_u32_e32 vcc, 0x200, v124
	s_and_saveexec_b64 s[16:17], vcc
	s_cbranch_execz .Lmk_end_b
	s_cmp_lt_u32 s8, 10
	s_cbranch_scc1 .Lmk_pos_only_b
	s_cmp_eq_u32 s8, 10
	s_cbranch_scc0 .Lmk_neg_only_b
	global_atomic_add_f32 v126, v127, s[4:5]
